# c3
# speedup vs baseline: 1.0236x; 1.0236x over previous
.LBB3_2:
	s_lshl_b32 s0, s39, 15
	s_add_i32 s0, s40, s0
	s_add_i32 s39, s0, 0x2000
	s_lshl_b32 s0, s41, 15
	v_bfe_u32 v3, v0, 4, 1
	s_add_i32 s0, s49, s0
	s_add_i32 s40, s0, 0x2000
	v_and_b32_e32 v8, 15, v0
	v_lshlrev_b32_e32 v10, 8, v3
	v_lshlrev_b32_e32 v3, 9, v3
	s_and_b32 s0, s33, 0xc0
	v_lshrrev_b32_e32 v1, 5, v1
	v_or3_b32 v3, s0, v3, v8
	v_lshlrev_b32_e32 v9, 15, v1
	v_lshl_add_u32 v11, s27, 7, v10
	v_mul_u32_u24_e32 v3, 24, v3
	s_waitcnt vmcnt(5)
	v_or_b32_e32 v11, v11, v8
	v_or3_b32 v8, v10, s0, v8
	v_or_b32_e32 v3, v3, v9
	s_add_i32 s41, 0, 0x10000
	s_addk_i32 s50, 0x2000
	v_lshl_add_u32 v11, v11, 4, v9
	v_lshlrev_b32_e32 v1, 10, v1
	v_lshlrev_b32_e32 v8, 1, v8
	v_add_u32_e32 v9, s41, v3
	s_barrier
	s_barrier
	s_add_u32 s72, s4, s22
	s_addc_u32 s73, s5, s23
	s_add_u32 s72, s72, s26
	s_addc_u32 s73, s73, 0
	s_add_u32 s72, s72, 0x8000
	s_addc_u32 s73, s73, 0
	s_add_u32 s74, s72, 0x4000
	s_addc_u32 s75, s73, 0
	s_add_u32 s76, s6, s24
	s_addc_u32 s77, s7, s25
	s_add_u32 s76, s76, 0xc000
	s_addc_u32 s77, s77, 0
	s_add_u32 s78, s76, 0xc000
	s_addc_u32 s79, s77, 0
	s_add_u32 s80, s14, s9
	s_addc_u32 s81, s15, 0
	s_add_u32 s80, s80, 0x800
	s_addc_u32 s81, s81, 0
	s_add_i32 s0, s38, s37
	s_add_i32 s0, s0, s26
	s_mulk_i32 s36, 0x1800
	s_sub_i32 s0, s0, s36
	s_addk_i32 s0, 0x4000
	v_lshl_add_u64 v[6:7], s[24:25], 0, v[6:7]
	s_ashr_i32 s1, s0, 31
	v_lshl_add_u64 v[142:143], v[6:7], 0, s[0:1]
	s_add_i32 s0, s35, s34
	s_add_i32 s0, s0, s26
	s_mulk_i32 s31, 0x1800
	s_sub_i32 s0, s0, s31
	s_addk_i32 s0, 0x2000
	s_ashr_i32 s1, s0, 31
	v_lshl_add_u64 v[144:145], v[6:7], 0, s[0:1]
	s_add_i32 s0, s30, s29
	s_add_i32 s0, s0, s26
	s_mulk_i32 s28, 0x1800
	s_sub_i32 s0, s0, s28
	s_ashr_i32 s1, s0, 31
	v_lshl_add_u64 v[146:147], v[6:7], 0, s[0:1]
	s_add_u32 s0, s4, s22
	s_addc_u32 s1, s5, s23
	v_lshl_add_u64 v[4:5], s[0:1], 0, v[4:5]
	s_mov_b64 s[0:1], 0xa000
	v_add_u32_e32 v3, 0, v3
	v_add3_u32 v248, 0, v8, v1
	v_lshl_add_u64 v[148:149], v[4:5], 0, s[0:1]
	s_movk_i32 s0, 0xa000
	s_movk_i32 s4, 0xc000
	s_add_i32 s57, s41, s50
	s_add_i32 s56, s41, s39
	s_add_i32 s55, s41, s40
	s_movk_i32 s28, 0xe000
	v_add_u32_e32 v171, 0x2000, v3
	v_add_u32_e32 v167, 0x3800, v3
	v_add_u32_e32 v162, 0x2000, v9
	v_add_u32_e32 v1, 0x3800, v9
	v_add_u32_e32 v174, 0x2180, v3
	v_add_u32_e32 v173, 0x2300, v3
	v_add_u32_e32 v172, 0x2480, v3
	v_add_u32_e32 v170, 0x3980, v3
	v_add_u32_e32 v169, 0x3b00, v3
	v_add_u32_e32 v168, 0x3c80, v3
	v_add_u32_e32 v165, 0x2180, v9
	v_add_u32_e32 v164, 0x2300, v9
	v_add_u32_e32 v163, 0x2480, v9
	v_add_u32_e32 v160, 0x3980, v9
	v_add_u32_e32 v159, 0x3b00, v9
	v_add_u32_e32 v158, 0x3c80, v9
	s_mov_b32 s59, -2
	s_movk_i32 s60, 0x1000
	v_add_u32_e32 v175, 0, v11
	s_mov_b32 s1, -1
	s_add_i32 s61, s41, s26
	s_mov_b32 s5, -1
	s_add_i32 s58, s13, 0x18000
	s_mov_b64 s[22:23], 0xc000
	s_mov_b64 s[24:25], 0x3000800
	s_mov_b64 s[26:27], 0xd800
	s_add_i32 s52, s57, 0x1800
	s_add_i32 s50, s56, 0x1800
	s_add_i32 s49, s55, 0x1800
	v_add_u32_e32 v166, s41, v11
	s_mov_b32 s29, -1
	s_mov_b64 s[30:31], 0x18000
	s_mov_b64 s[34:35], 0x3001000
	s_mov_b64 s[36:37], 0x19800
	s_mov_b64 s[38:39], 0x1000
	s_mov_b64 s[40:41], 0x8000
	v_mov_b32_e32 v3, v2
	v_mov_b32_e32 v4, v2
	v_mov_b32_e32 v5, v2
	v_mov_b32_e32 v10, v2
	v_mov_b32_e32 v11, v2
	v_mov_b32_e32 v12, v2
	v_mov_b32_e32 v13, v2
	v_mov_b32_e32 v22, v2
	v_mov_b32_e32 v23, v2
	v_mov_b32_e32 v24, v2
	v_mov_b32_e32 v25, v2
	v_mov_b32_e32 v38, v2
	v_mov_b32_e32 v39, v2
	v_mov_b32_e32 v40, v2
	v_mov_b32_e32 v41, v2
	v_mov_b32_e32 v6, v2
	v_mov_b32_e32 v7, v2
	v_mov_b32_e32 v8, v2
	v_mov_b32_e32 v9, v2
	v_mov_b32_e32 v18, v2
	v_mov_b32_e32 v19, v2
	v_mov_b32_e32 v20, v2
	v_mov_b32_e32 v21, v2
	v_mov_b32_e32 v34, v2
	v_mov_b32_e32 v35, v2
	v_mov_b32_e32 v36, v2
	v_mov_b32_e32 v37, v2
	v_mov_b32_e32 v54, v2
	v_mov_b32_e32 v55, v2
	v_mov_b32_e32 v56, v2
	v_mov_b32_e32 v57, v2
	v_mov_b32_e32 v14, v2
	v_mov_b32_e32 v15, v2
	v_mov_b32_e32 v16, v2
	v_mov_b32_e32 v17, v2
	v_mov_b32_e32 v30, v2
	v_mov_b32_e32 v31, v2
	v_mov_b32_e32 v32, v2
	v_mov_b32_e32 v33, v2
	v_mov_b32_e32 v50, v2
	v_mov_b32_e32 v51, v2
	v_mov_b32_e32 v52, v2
	v_mov_b32_e32 v53, v2
	v_mov_b32_e32 v70, v2
	v_mov_b32_e32 v71, v2
	v_mov_b32_e32 v72, v2
	v_mov_b32_e32 v73, v2
	v_mov_b32_e32 v26, v2
	v_mov_b32_e32 v27, v2
	v_mov_b32_e32 v28, v2
	v_mov_b32_e32 v29, v2
	v_mov_b32_e32 v46, v2
	v_mov_b32_e32 v47, v2
	v_mov_b32_e32 v48, v2
	v_mov_b32_e32 v49, v2
	v_mov_b32_e32 v66, v2
	v_mov_b32_e32 v67, v2
	v_mov_b32_e32 v68, v2
	v_mov_b32_e32 v69, v2
	v_mov_b32_e32 v86, v2
	v_mov_b32_e32 v87, v2
	v_mov_b32_e32 v88, v2
	v_mov_b32_e32 v89, v2
	v_mov_b32_e32 v42, v2
	v_mov_b32_e32 v43, v2
	v_mov_b32_e32 v44, v2
	v_mov_b32_e32 v45, v2
	v_mov_b32_e32 v62, v2
	v_mov_b32_e32 v63, v2
	v_mov_b32_e32 v64, v2
	v_mov_b32_e32 v65, v2
	v_mov_b32_e32 v82, v2
	v_mov_b32_e32 v83, v2
	v_mov_b32_e32 v84, v2
	v_mov_b32_e32 v85, v2
	v_mov_b32_e32 v102, v2
	v_mov_b32_e32 v103, v2
	v_mov_b32_e32 v104, v2
	v_mov_b32_e32 v105, v2
	v_mov_b32_e32 v58, v2
	v_mov_b32_e32 v59, v2
	v_mov_b32_e32 v60, v2
	v_mov_b32_e32 v61, v2
	v_mov_b32_e32 v78, v2
	v_mov_b32_e32 v79, v2
	v_mov_b32_e32 v80, v2
	v_mov_b32_e32 v81, v2
	v_mov_b32_e32 v98, v2
	v_mov_b32_e32 v99, v2
	v_mov_b32_e32 v100, v2
	v_mov_b32_e32 v101, v2
	v_mov_b32_e32 v114, v2
	v_mov_b32_e32 v115, v2
	v_mov_b32_e32 v116, v2
	v_mov_b32_e32 v117, v2
	v_mov_b32_e32 v74, v2
	v_mov_b32_e32 v75, v2
	v_mov_b32_e32 v76, v2
	v_mov_b32_e32 v77, v2
	v_mov_b32_e32 v94, v2
	v_mov_b32_e32 v95, v2
	v_mov_b32_e32 v96, v2
	v_mov_b32_e32 v97, v2
	v_mov_b32_e32 v110, v2
	v_mov_b32_e32 v111, v2
	v_mov_b32_e32 v112, v2
	v_mov_b32_e32 v113, v2
	v_mov_b32_e32 v122, v2
	v_mov_b32_e32 v123, v2
	v_mov_b32_e32 v124, v2
	v_mov_b32_e32 v125, v2
	v_mov_b32_e32 v90, v2
	v_mov_b32_e32 v91, v2
	v_mov_b32_e32 v92, v2
	v_mov_b32_e32 v93, v2
	v_mov_b32_e32 v106, v2
	v_mov_b32_e32 v107, v2
	v_mov_b32_e32 v108, v2
	v_mov_b32_e32 v109, v2
	v_mov_b32_e32 v118, v2
	v_mov_b32_e32 v119, v2
	v_mov_b32_e32 v120, v2
	v_mov_b32_e32 v121, v2
	v_mov_b32_e32 v126, v2
	v_mov_b32_e32 v127, v2
	v_mov_b32_e32 v128, v2
	v_mov_b32_e32 v129, v2
	v_add_u32_e32 v176, 0x20000, v248
	v_mov_b32_e32 v177, 0x7f7f7f7f
	v_lshl_add_u64 v[150:151], s[42:43], 0, v[130:131]
	s_mov_b64 s[62:63], 0x2000
	s_mov_b64 s[64:65], 0x4000
	v_and_b32_e32 v142, 63, v0
	v_lshlrev_b32_e32 v150, 2, v142
	v_lshlrev_b32_e32 v142, 4, v142
	v_add_u32_e32 v143, 0x2000, v142
	v_add_u32_e32 v144, s16, v142
	v_add_u32_e32 v145, s18, v142
	v_add_u32_e32 v146, s20, v142
	v_add_u32_e32 v147, 0x1800, v144
	v_add_u32_e32 v148, 0x1800, v145
	v_add_u32_e32 v149, 0x1800, v146
	v_add_u32_e32 v151, 0x800, v150
.LBB3_3:
	ds_read_b128 v[202:205], v175
	ds_read_b128 v[206:209], v175 offset:256
	ds_read_b128 v[210:213], v175 offset:512
	ds_read_b128 v[214:217], v175 offset:768
	ds_read_b128 v[218:221], v175 offset:1024
	ds_read_b128 v[222:225], v175 offset:1280
	ds_read_b128 v[226:229], v175 offset:1536
	ds_read_b128 v[230:233], v175 offset:1792
	ds_read_b64 v[178:179], v171
	ds_read_b64 v[180:181], v171 offset:8
	ds_read_b64 v[182:183], v171 offset:16
	ds_read_b64 v[184:185], v174
	ds_read_b64 v[186:187], v174 offset:8
	ds_read_b64 v[188:189], v174 offset:16
	s_add_i32 s42, s60, 0xfffff000
	ds_read_b64 v[190:191], v173
	ds_read_b64 v[192:193], v173 offset:8
	ds_read_b64 v[194:195], v173 offset:16
	s_and_b32 s42, s42, 0x1000
	ds_read_b64 v[196:197], v172
	ds_read_b64 v[198:199], v172 offset:8
	ds_read_b64 v[200:201], v172 offset:16
	v_add_u32_e32 v152, s42, v176
	ds_read_u16 v240, v152
	ds_read_u16 v241, v152 offset:32
	ds_read_u16 v242, v152 offset:64
	ds_read_u16 v243, v152 offset:96
	s_add_i32 s42, s60, 0xfffff800
	s_mov_b32 m0, s57
	s_nop 0
	global_load_lds_dwordx4 v144, s[76:77]
	s_mov_b32 m0, s56
	s_and_b32 s42, s42, 0x1800
	global_load_lds_dwordx4 v145, s[76:77]
	s_mov_b32 m0, s55
	s_nop 0
	global_load_lds_dwordx4 v146, s[76:77]
	s_add_i32 m0, s48, s42
	s_nop 0
	global_load_lds_dword v150, s[80:81]
	s_waitcnt vmcnt(6)
	s_waitcnt lgkmcnt(0)
	s_barrier
	v_mfma_scale_f32_16x16x128_f8f6f4 v[126:129], v[202:205], v[178:183], v[126:129], v177, v240 op_sel_hi:[0,0,0] cbsz:4 blgp:2
	v_mfma_scale_f32_16x16x128_f8f6f4 v[122:125], v[206:209], v[178:183], v[122:125], v177, v240 op_sel_hi:[0,0,0] cbsz:4 blgp:2
	v_mfma_scale_f32_16x16x128_f8f6f4 v[114:117], v[210:213], v[178:183], v[114:117], v177, v240 op_sel_hi:[0,0,0] cbsz:4 blgp:2
	v_mfma_scale_f32_16x16x128_f8f6f4 v[102:105], v[214:217], v[178:183], v[102:105], v177, v240 op_sel_hi:[0,0,0] cbsz:4 blgp:2
	v_mfma_scale_f32_16x16x128_f8f6f4 v[86:89], v[218:221], v[178:183], v[86:89], v177, v240 op_sel_hi:[0,0,0] cbsz:4 blgp:2
	v_mfma_scale_f32_16x16x128_f8f6f4 v[70:73], v[222:225], v[178:183], v[70:73], v177, v240 op_sel_hi:[0,0,0] cbsz:4 blgp:2
	v_mfma_scale_f32_16x16x128_f8f6f4 v[54:57], v[226:229], v[178:183], v[54:57], v177, v240 op_sel_hi:[0,0,0] cbsz:4 blgp:2
	v_mfma_scale_f32_16x16x128_f8f6f4 v[38:41], v[230:233], v[178:183], v[38:41], v177, v240 op_sel_hi:[0,0,0] cbsz:4 blgp:2
	v_mfma_scale_f32_16x16x128_f8f6f4 v[118:121], v[202:205], v[184:189], v[118:121], v177, v241 op_sel_hi:[0,0,0] cbsz:4 blgp:2
	v_mfma_scale_f32_16x16x128_f8f6f4 v[110:113], v[206:209], v[184:189], v[110:113], v177, v241 op_sel_hi:[0,0,0] cbsz:4 blgp:2
	v_mfma_scale_f32_16x16x128_f8f6f4 v[98:101], v[210:213], v[184:189], v[98:101], v177, v241 op_sel_hi:[0,0,0] cbsz:4 blgp:2
	v_mfma_scale_f32_16x16x128_f8f6f4 v[82:85], v[214:217], v[184:189], v[82:85], v177, v241 op_sel_hi:[0,0,0] cbsz:4 blgp:2
	v_mfma_scale_f32_16x16x128_f8f6f4 v[66:69], v[218:221], v[184:189], v[66:69], v177, v241 op_sel_hi:[0,0,0] cbsz:4 blgp:2
	v_mfma_scale_f32_16x16x128_f8f6f4 v[50:53], v[222:225], v[184:189], v[50:53], v177, v241 op_sel_hi:[0,0,0] cbsz:4 blgp:2
	v_mfma_scale_f32_16x16x128_f8f6f4 v[34:37], v[226:229], v[184:189], v[34:37], v177, v241 op_sel_hi:[0,0,0] cbsz:4 blgp:2
	v_mfma_scale_f32_16x16x128_f8f6f4 v[106:109], v[202:205], v[190:195], v[106:109], v177, v242 op_sel_hi:[0,0,0] cbsz:4 blgp:2
	v_mfma_scale_f32_16x16x128_f8f6f4 v[94:97], v[206:209], v[190:195], v[94:97], v177, v242 op_sel_hi:[0,0,0] cbsz:4 blgp:2
	v_mfma_scale_f32_16x16x128_f8f6f4 v[78:81], v[210:213], v[190:195], v[78:81], v177, v242 op_sel_hi:[0,0,0] cbsz:4 blgp:2
	v_mfma_scale_f32_16x16x128_f8f6f4 v[62:65], v[214:217], v[190:195], v[62:65], v177, v242 op_sel_hi:[0,0,0] cbsz:4 blgp:2
	v_mfma_scale_f32_16x16x128_f8f6f4 v[46:49], v[218:221], v[190:195], v[46:49], v177, v242 op_sel_hi:[0,0,0] cbsz:4 blgp:2
	v_mfma_scale_f32_16x16x128_f8f6f4 v[30:33], v[222:225], v[190:195], v[30:33], v177, v242 op_sel_hi:[0,0,0] cbsz:4 blgp:2
	v_mfma_scale_f32_16x16x128_f8f6f4 v[90:93], v[202:205], v[196:201], v[90:93], v177, v243 op_sel_hi:[0,0,0] cbsz:4 blgp:2
	v_mfma_scale_f32_16x16x128_f8f6f4 v[74:77], v[206:209], v[196:201], v[74:77], v177, v243 op_sel_hi:[0,0,0] cbsz:4 blgp:2
	v_mfma_scale_f32_16x16x128_f8f6f4 v[58:61], v[210:213], v[196:201], v[58:61], v177, v243 op_sel_hi:[0,0,0] cbsz:4 blgp:2
	v_mfma_scale_f32_16x16x128_f8f6f4 v[42:45], v[214:217], v[196:201], v[42:45], v177, v243 op_sel_hi:[0,0,0] cbsz:4 blgp:2
	v_mfma_scale_f32_16x16x128_f8f6f4 v[26:29], v[218:221], v[196:201], v[26:29], v177, v243 op_sel_hi:[0,0,0] cbsz:4 blgp:2
	v_mfma_scale_f32_16x16x128_f8f6f4 v[178:181], v[230:233], v[184:189], v[22:25], v177, v241 op_sel_hi:[0,0,0] cbsz:4 blgp:2
	v_mfma_scale_f32_16x16x128_f8f6f4 v[182:185], v[226:229], v[190:195], v[18:21], v177, v242 op_sel_hi:[0,0,0] cbsz:4 blgp:2
	v_mfma_scale_f32_16x16x128_f8f6f4 v[186:189], v[230:233], v[190:195], v[10:13], v177, v242 op_sel_hi:[0,0,0] cbsz:4 blgp:2
	v_mfma_scale_f32_16x16x128_f8f6f4 v[190:193], v[222:225], v[196:201], v[14:17], v177, v243 op_sel_hi:[0,0,0] cbsz:4 blgp:2
	v_mfma_scale_f32_16x16x128_f8f6f4 v[234:237], v[226:229], v[196:201], v[6:9], v177, v243 op_sel_hi:[0,0,0] cbsz:4 blgp:2
	v_mfma_scale_f32_16x16x128_f8f6f4 v[194:197], v[230:233], v[196:201], v[2:5], v177, v243 op_sel_hi:[0,0,0] cbsz:4 blgp:2
	s_barrier
	ds_read_b64 v[2:3], v167
	ds_read_b64 v[4:5], v167 offset:8
	ds_read_b64 v[6:7], v167 offset:16
	ds_read_b64 v[8:9], v170
	ds_read_b64 v[10:11], v170 offset:8
	ds_read_b64 v[12:13], v170 offset:16
	ds_read_b64 v[14:15], v169
	ds_read_b64 v[16:17], v169 offset:8
	ds_read_b64 v[18:19], v169 offset:16
	s_mov_b32 m0, s52
	ds_read_b64 v[20:21], v168
	ds_read_b64 v[22:23], v168 offset:8
	ds_read_b64 v[24:25], v168 offset:16
	global_load_lds_dwordx4 v147, s[76:77]
	s_mov_b32 m0, s50
	s_nop 0
	global_load_lds_dwordx4 v148, s[76:77]
	s_mov_b32 m0, s49
	s_nop 0
	global_load_lds_dwordx4 v149, s[76:77]
	s_mov_b32 m0, s13
	s_nop 0
	global_load_lds_dwordx4 v142, s[72:73]
	s_mov_b32 m0, s44
	s_nop 0
	global_load_lds_dwordx4 v143, s[72:73]
	s_waitcnt vmcnt(5)
	s_waitcnt lgkmcnt(0)
	s_barrier
	v_mfma_scale_f32_16x16x128_f8f6f4 v[126:129], v[202:205], v[2:7], v[126:129], v177, v240 op_sel:[0,1,0] op_sel_hi:[0,0,0] cbsz:4 blgp:2
	v_mfma_scale_f32_16x16x128_f8f6f4 v[122:125], v[206:209], v[2:7], v[122:125], v177, v240 op_sel:[0,1,0] op_sel_hi:[0,0,0] cbsz:4 blgp:2
	v_mfma_scale_f32_16x16x128_f8f6f4 v[114:117], v[210:213], v[2:7], v[114:117], v177, v240 op_sel:[0,1,0] op_sel_hi:[0,0,0] cbsz:4 blgp:2
	v_mfma_scale_f32_16x16x128_f8f6f4 v[102:105], v[214:217], v[2:7], v[102:105], v177, v240 op_sel:[0,1,0] op_sel_hi:[0,0,0] cbsz:4 blgp:2
	v_mfma_scale_f32_16x16x128_f8f6f4 v[86:89], v[218:221], v[2:7], v[86:89], v177, v240 op_sel:[0,1,0] op_sel_hi:[0,0,0] cbsz:4 blgp:2
	v_mfma_scale_f32_16x16x128_f8f6f4 v[70:73], v[222:225], v[2:7], v[70:73], v177, v240 op_sel:[0,1,0] op_sel_hi:[0,0,0] cbsz:4 blgp:2
	v_mfma_scale_f32_16x16x128_f8f6f4 v[54:57], v[226:229], v[2:7], v[54:57], v177, v240 op_sel:[0,1,0] op_sel_hi:[0,0,0] cbsz:4 blgp:2
	v_mfma_scale_f32_16x16x128_f8f6f4 v[38:41], v[230:233], v[2:7], v[38:41], v177, v240 op_sel:[0,1,0] op_sel_hi:[0,0,0] cbsz:4 blgp:2
	v_mfma_scale_f32_16x16x128_f8f6f4 v[118:121], v[202:205], v[8:13], v[118:121], v177, v241 op_sel:[0,1,0] op_sel_hi:[0,0,0] cbsz:4 blgp:2
	v_mfma_scale_f32_16x16x128_f8f6f4 v[110:113], v[206:209], v[8:13], v[110:113], v177, v241 op_sel:[0,1,0] op_sel_hi:[0,0,0] cbsz:4 blgp:2
	v_mfma_scale_f32_16x16x128_f8f6f4 v[98:101], v[210:213], v[8:13], v[98:101], v177, v241 op_sel:[0,1,0] op_sel_hi:[0,0,0] cbsz:4 blgp:2
	v_mfma_scale_f32_16x16x128_f8f6f4 v[82:85], v[214:217], v[8:13], v[82:85], v177, v241 op_sel:[0,1,0] op_sel_hi:[0,0,0] cbsz:4 blgp:2
	v_mfma_scale_f32_16x16x128_f8f6f4 v[66:69], v[218:221], v[8:13], v[66:69], v177, v241 op_sel:[0,1,0] op_sel_hi:[0,0,0] cbsz:4 blgp:2
	v_mfma_scale_f32_16x16x128_f8f6f4 v[50:53], v[222:225], v[8:13], v[50:53], v177, v241 op_sel:[0,1,0] op_sel_hi:[0,0,0] cbsz:4 blgp:2
	v_mfma_scale_f32_16x16x128_f8f6f4 v[34:37], v[226:229], v[8:13], v[34:37], v177, v241 op_sel:[0,1,0] op_sel_hi:[0,0,0] cbsz:4 blgp:2
	v_mfma_scale_f32_16x16x128_f8f6f4 v[106:109], v[202:205], v[14:19], v[106:109], v177, v242 op_sel:[0,1,0] op_sel_hi:[0,0,0] cbsz:4 blgp:2
	v_mfma_scale_f32_16x16x128_f8f6f4 v[94:97], v[206:209], v[14:19], v[94:97], v177, v242 op_sel:[0,1,0] op_sel_hi:[0,0,0] cbsz:4 blgp:2
	v_mfma_scale_f32_16x16x128_f8f6f4 v[78:81], v[210:213], v[14:19], v[78:81], v177, v242 op_sel:[0,1,0] op_sel_hi:[0,0,0] cbsz:4 blgp:2
	v_mfma_scale_f32_16x16x128_f8f6f4 v[62:65], v[214:217], v[14:19], v[62:65], v177, v242 op_sel:[0,1,0] op_sel_hi:[0,0,0] cbsz:4 blgp:2
	v_mfma_scale_f32_16x16x128_f8f6f4 v[46:49], v[218:221], v[14:19], v[46:49], v177, v242 op_sel:[0,1,0] op_sel_hi:[0,0,0] cbsz:4 blgp:2
	v_mfma_scale_f32_16x16x128_f8f6f4 v[30:33], v[222:225], v[14:19], v[30:33], v177, v242 op_sel:[0,1,0] op_sel_hi:[0,0,0] cbsz:4 blgp:2
	v_mfma_scale_f32_16x16x128_f8f6f4 v[90:93], v[202:205], v[20:25], v[90:93], v177, v243 op_sel:[0,1,0] op_sel_hi:[0,0,0] cbsz:4 blgp:2
	v_mfma_scale_f32_16x16x128_f8f6f4 v[74:77], v[206:209], v[20:25], v[74:77], v177, v243 op_sel:[0,1,0] op_sel_hi:[0,0,0] cbsz:4 blgp:2
	v_mfma_scale_f32_16x16x128_f8f6f4 v[58:61], v[210:213], v[20:25], v[58:61], v177, v243 op_sel:[0,1,0] op_sel_hi:[0,0,0] cbsz:4 blgp:2
	v_mfma_scale_f32_16x16x128_f8f6f4 v[42:45], v[214:217], v[20:25], v[42:45], v177, v243 op_sel:[0,1,0] op_sel_hi:[0,0,0] cbsz:4 blgp:2
	v_mfma_scale_f32_16x16x128_f8f6f4 v[26:29], v[218:221], v[20:25], v[26:29], v177, v243 op_sel:[0,1,0] op_sel_hi:[0,0,0] cbsz:4 blgp:2
	v_mfma_scale_f32_16x16x128_f8f6f4 v[178:181], v[230:233], v[8:13], v[178:181], v177, v241 op_sel:[0,1,0] op_sel_hi:[0,0,0] cbsz:4 blgp:2
	v_mfma_scale_f32_16x16x128_f8f6f4 v[182:185], v[226:229], v[14:19], v[182:185], v177, v242 op_sel:[0,1,0] op_sel_hi:[0,0,0] cbsz:4 blgp:2
	v_mfma_scale_f32_16x16x128_f8f6f4 v[186:189], v[230:233], v[14:19], v[186:189], v177, v242 op_sel:[0,1,0] op_sel_hi:[0,0,0] cbsz:4 blgp:2
	v_mfma_scale_f32_16x16x128_f8f6f4 v[190:193], v[222:225], v[20:25], v[190:193], v177, v243 op_sel:[0,1,0] op_sel_hi:[0,0,0] cbsz:4 blgp:2
	v_mfma_scale_f32_16x16x128_f8f6f4 v[198:201], v[226:229], v[20:25], v[234:237], v177, v243 op_sel:[0,1,0] op_sel_hi:[0,0,0] cbsz:4 blgp:2
	v_mfma_scale_f32_16x16x128_f8f6f4 v[194:197], v[230:233], v[20:25], v[194:197], v177, v243 op_sel:[0,1,0] op_sel_hi:[0,0,0] cbsz:4 blgp:2
	s_barrier
	ds_read_b128 v[202:205], v166
	ds_read_b128 v[206:209], v166 offset:256
	ds_read_b128 v[210:213], v166 offset:512
	ds_read_b128 v[214:217], v166 offset:768
	ds_read_b128 v[218:221], v166 offset:1024
	ds_read_b128 v[222:225], v166 offset:1280
	ds_read_b128 v[226:229], v166 offset:1536
	ds_read_b128 v[230:233], v166 offset:1792
	ds_read_b64 v[2:3], v162
	ds_read_b64 v[4:5], v162 offset:8
	ds_read_b64 v[6:7], v162 offset:16
	ds_read_b64 v[8:9], v165
	ds_read_b64 v[10:11], v165 offset:8
	ds_read_b64 v[12:13], v165 offset:16
	ds_read_b64 v[14:15], v164
	ds_read_b64 v[16:17], v164 offset:8
	ds_read_b64 v[18:19], v164 offset:16
	ds_read_b64 v[20:21], v163
	ds_read_b64 v[22:23], v163 offset:8
	ds_read_b64 v[24:25], v163 offset:16
	v_add_u32_e32 v234, s42, v176
	ds_read_u16 v242, v234
	ds_read_u16 v243, v234 offset:32
	ds_read_u16 v244, v234 offset:64
	ds_read_u16 v245, v234 offset:96
	s_mov_b32 m0, s45
	s_and_b32 s42, s60, 0x1000
	global_load_lds_dwordx4 v144, s[78:79]
	s_mov_b32 m0, s46
	s_nop 0
	global_load_lds_dwordx4 v145, s[78:79]
	s_mov_b32 m0, s47
	s_nop 0
	global_load_lds_dwordx4 v146, s[78:79]
	s_add_i32 m0, s48, s42
	s_nop 0
	global_load_lds_dword v151, s[80:81]
	s_waitcnt vmcnt(6)
	s_waitcnt lgkmcnt(0)
	s_barrier
	v_mfma_scale_f32_16x16x128_f8f6f4 v[126:129], v[202:205], v[2:7], v[126:129], v177, v242 op_sel_hi:[0,0,0] cbsz:4 blgp:2
	v_mfma_scale_f32_16x16x128_f8f6f4 v[122:125], v[206:209], v[2:7], v[122:125], v177, v242 op_sel_hi:[0,0,0] cbsz:4 blgp:2
	v_mfma_scale_f32_16x16x128_f8f6f4 v[114:117], v[210:213], v[2:7], v[114:117], v177, v242 op_sel_hi:[0,0,0] cbsz:4 blgp:2
	v_mfma_scale_f32_16x16x128_f8f6f4 v[102:105], v[214:217], v[2:7], v[102:105], v177, v242 op_sel_hi:[0,0,0] cbsz:4 blgp:2
	v_mfma_scale_f32_16x16x128_f8f6f4 v[86:89], v[218:221], v[2:7], v[86:89], v177, v242 op_sel_hi:[0,0,0] cbsz:4 blgp:2
	v_mfma_scale_f32_16x16x128_f8f6f4 v[70:73], v[222:225], v[2:7], v[70:73], v177, v242 op_sel_hi:[0,0,0] cbsz:4 blgp:2
	v_mfma_scale_f32_16x16x128_f8f6f4 v[54:57], v[226:229], v[2:7], v[54:57], v177, v242 op_sel_hi:[0,0,0] cbsz:4 blgp:2
	v_mfma_scale_f32_16x16x128_f8f6f4 v[38:41], v[230:233], v[2:7], v[38:41], v177, v242 op_sel_hi:[0,0,0] cbsz:4 blgp:2
	v_mfma_scale_f32_16x16x128_f8f6f4 v[118:121], v[202:205], v[8:13], v[118:121], v177, v243 op_sel_hi:[0,0,0] cbsz:4 blgp:2
	v_mfma_scale_f32_16x16x128_f8f6f4 v[110:113], v[206:209], v[8:13], v[110:113], v177, v243 op_sel_hi:[0,0,0] cbsz:4 blgp:2
	v_mfma_scale_f32_16x16x128_f8f6f4 v[98:101], v[210:213], v[8:13], v[98:101], v177, v243 op_sel_hi:[0,0,0] cbsz:4 blgp:2
	v_mfma_scale_f32_16x16x128_f8f6f4 v[82:85], v[214:217], v[8:13], v[82:85], v177, v243 op_sel_hi:[0,0,0] cbsz:4 blgp:2
	v_mfma_scale_f32_16x16x128_f8f6f4 v[66:69], v[218:221], v[8:13], v[66:69], v177, v243 op_sel_hi:[0,0,0] cbsz:4 blgp:2
	v_mfma_scale_f32_16x16x128_f8f6f4 v[50:53], v[222:225], v[8:13], v[50:53], v177, v243 op_sel_hi:[0,0,0] cbsz:4 blgp:2
	v_mfma_scale_f32_16x16x128_f8f6f4 v[34:37], v[226:229], v[8:13], v[34:37], v177, v243 op_sel_hi:[0,0,0] cbsz:4 blgp:2
	v_mfma_scale_f32_16x16x128_f8f6f4 v[106:109], v[202:205], v[14:19], v[106:109], v177, v244 op_sel_hi:[0,0,0] cbsz:4 blgp:2
	v_mfma_scale_f32_16x16x128_f8f6f4 v[94:97], v[206:209], v[14:19], v[94:97], v177, v244 op_sel_hi:[0,0,0] cbsz:4 blgp:2
	v_mfma_scale_f32_16x16x128_f8f6f4 v[78:81], v[210:213], v[14:19], v[78:81], v177, v244 op_sel_hi:[0,0,0] cbsz:4 blgp:2
	v_mfma_scale_f32_16x16x128_f8f6f4 v[62:65], v[214:217], v[14:19], v[62:65], v177, v244 op_sel_hi:[0,0,0] cbsz:4 blgp:2
	v_mfma_scale_f32_16x16x128_f8f6f4 v[46:49], v[218:221], v[14:19], v[46:49], v177, v244 op_sel_hi:[0,0,0] cbsz:4 blgp:2
	v_mfma_scale_f32_16x16x128_f8f6f4 v[30:33], v[222:225], v[14:19], v[30:33], v177, v244 op_sel_hi:[0,0,0] cbsz:4 blgp:2
	v_mfma_scale_f32_16x16x128_f8f6f4 v[238:241], v[226:229], v[14:19], v[182:185], v177, v244 op_sel_hi:[0,0,0] cbsz:4 blgp:2
	v_mfma_scale_f32_16x16x128_f8f6f4 v[14:17], v[230:233], v[14:19], v[186:189], v177, v244 op_sel_hi:[0,0,0] cbsz:4 blgp:2
	v_mfma_scale_f32_16x16x128_f8f6f4 v[90:93], v[202:205], v[20:25], v[90:93], v177, v245 op_sel_hi:[0,0,0] cbsz:4 blgp:2
	v_mfma_scale_f32_16x16x128_f8f6f4 v[74:77], v[206:209], v[20:25], v[74:77], v177, v245 op_sel_hi:[0,0,0] cbsz:4 blgp:2
	v_mfma_scale_f32_16x16x128_f8f6f4 v[58:61], v[210:213], v[20:25], v[58:61], v177, v245 op_sel_hi:[0,0,0] cbsz:4 blgp:2
	v_mfma_scale_f32_16x16x128_f8f6f4 v[42:45], v[214:217], v[20:25], v[42:45], v177, v245 op_sel_hi:[0,0,0] cbsz:4 blgp:2
	v_mfma_scale_f32_16x16x128_f8f6f4 v[26:29], v[218:221], v[20:25], v[26:29], v177, v245 op_sel_hi:[0,0,0] cbsz:4 blgp:2
	v_mfma_scale_f32_16x16x128_f8f6f4 v[234:237], v[230:233], v[8:13], v[178:181], v177, v243 op_sel_hi:[0,0,0] cbsz:4 blgp:2
	v_mfma_scale_f32_16x16x128_f8f6f4 v[190:193], v[222:225], v[20:25], v[190:193], v177, v245 op_sel_hi:[0,0,0] cbsz:4 blgp:2
	v_mfma_scale_f32_16x16x128_f8f6f4 v[198:201], v[226:229], v[20:25], v[198:201], v177, v245 op_sel_hi:[0,0,0] cbsz:4 blgp:2
	v_mfma_scale_f32_16x16x128_f8f6f4 v[194:197], v[230:233], v[20:25], v[194:197], v177, v245 op_sel_hi:[0,0,0] cbsz:4 blgp:2
	s_barrier
	ds_read_b64 v[2:3], v1
	ds_read_b64 v[4:5], v1 offset:8
	ds_read_b64 v[6:7], v1 offset:16
	ds_read_b64 v[8:9], v160
	ds_read_b64 v[10:11], v160 offset:8
	ds_read_b64 v[12:13], v160 offset:16
	ds_read_b64 v[178:179], v159
	ds_read_b64 v[180:181], v159 offset:8
	ds_read_b64 v[182:183], v159 offset:16
	s_mov_b32 m0, s51
	ds_read_b64 v[184:185], v158
	ds_read_b64 v[186:187], v158 offset:8
	ds_read_b64 v[188:189], v158 offset:16
	global_load_lds_dwordx4 v147, s[78:79]
	s_mov_b32 m0, s53
	s_nop 0
	global_load_lds_dwordx4 v148, s[78:79]
	s_mov_b32 m0, s54
	s_nop 0
	global_load_lds_dwordx4 v149, s[78:79]
	s_mov_b32 m0, s61
	s_nop 0
	global_load_lds_dwordx4 v142, s[74:75]
	s_mov_b32 m0, s58
	s_nop 0
	global_load_lds_dwordx4 v143, s[74:75]
	s_waitcnt vmcnt(5)
	s_waitcnt lgkmcnt(0)
	s_barrier
	v_mfma_scale_f32_16x16x128_f8f6f4 v[126:129], v[202:205], v[2:7], v[126:129], v177, v242 op_sel:[0,1,0] op_sel_hi:[0,0,0] cbsz:4 blgp:2
	v_mfma_scale_f32_16x16x128_f8f6f4 v[122:125], v[206:209], v[2:7], v[122:125], v177, v242 op_sel:[0,1,0] op_sel_hi:[0,0,0] cbsz:4 blgp:2
	v_mfma_scale_f32_16x16x128_f8f6f4 v[114:117], v[210:213], v[2:7], v[114:117], v177, v242 op_sel:[0,1,0] op_sel_hi:[0,0,0] cbsz:4 blgp:2
	v_mfma_scale_f32_16x16x128_f8f6f4 v[102:105], v[214:217], v[2:7], v[102:105], v177, v242 op_sel:[0,1,0] op_sel_hi:[0,0,0] cbsz:4 blgp:2
	v_mfma_scale_f32_16x16x128_f8f6f4 v[86:89], v[218:221], v[2:7], v[86:89], v177, v242 op_sel:[0,1,0] op_sel_hi:[0,0,0] cbsz:4 blgp:2
	v_mfma_scale_f32_16x16x128_f8f6f4 v[70:73], v[222:225], v[2:7], v[70:73], v177, v242 op_sel:[0,1,0] op_sel_hi:[0,0,0] cbsz:4 blgp:2
	v_mfma_scale_f32_16x16x128_f8f6f4 v[54:57], v[226:229], v[2:7], v[54:57], v177, v242 op_sel:[0,1,0] op_sel_hi:[0,0,0] cbsz:4 blgp:2
	v_mfma_scale_f32_16x16x128_f8f6f4 v[38:41], v[230:233], v[2:7], v[38:41], v177, v242 op_sel:[0,1,0] op_sel_hi:[0,0,0] cbsz:4 blgp:2
	v_mfma_scale_f32_16x16x128_f8f6f4 v[118:121], v[202:205], v[8:13], v[118:121], v177, v243 op_sel:[0,1,0] op_sel_hi:[0,0,0] cbsz:4 blgp:2
	v_mfma_scale_f32_16x16x128_f8f6f4 v[110:113], v[206:209], v[8:13], v[110:113], v177, v243 op_sel:[0,1,0] op_sel_hi:[0,0,0] cbsz:4 blgp:2
	v_mfma_scale_f32_16x16x128_f8f6f4 v[98:101], v[210:213], v[8:13], v[98:101], v177, v243 op_sel:[0,1,0] op_sel_hi:[0,0,0] cbsz:4 blgp:2
	v_mfma_scale_f32_16x16x128_f8f6f4 v[82:85], v[214:217], v[8:13], v[82:85], v177, v243 op_sel:[0,1,0] op_sel_hi:[0,0,0] cbsz:4 blgp:2
	v_mfma_scale_f32_16x16x128_f8f6f4 v[66:69], v[218:221], v[8:13], v[66:69], v177, v243 op_sel:[0,1,0] op_sel_hi:[0,0,0] cbsz:4 blgp:2
	v_mfma_scale_f32_16x16x128_f8f6f4 v[50:53], v[222:225], v[8:13], v[50:53], v177, v243 op_sel:[0,1,0] op_sel_hi:[0,0,0] cbsz:4 blgp:2
	v_mfma_scale_f32_16x16x128_f8f6f4 v[34:37], v[226:229], v[8:13], v[34:37], v177, v243 op_sel:[0,1,0] op_sel_hi:[0,0,0] cbsz:4 blgp:2
	v_mfma_scale_f32_16x16x128_f8f6f4 v[22:25], v[230:233], v[8:13], v[234:237], v177, v243 op_sel:[0,1,0] op_sel_hi:[0,0,0] cbsz:4 blgp:2
	v_mfma_scale_f32_16x16x128_f8f6f4 v[106:109], v[202:205], v[178:183], v[106:109], v177, v244 op_sel:[0,1,0] op_sel_hi:[0,0,0] cbsz:4 blgp:2
	v_mfma_scale_f32_16x16x128_f8f6f4 v[94:97], v[206:209], v[178:183], v[94:97], v177, v244 op_sel:[0,1,0] op_sel_hi:[0,0,0] cbsz:4 blgp:2
	v_mfma_scale_f32_16x16x128_f8f6f4 v[78:81], v[210:213], v[178:183], v[78:81], v177, v244 op_sel:[0,1,0] op_sel_hi:[0,0,0] cbsz:4 blgp:2
	v_mfma_scale_f32_16x16x128_f8f6f4 v[62:65], v[214:217], v[178:183], v[62:65], v177, v244 op_sel:[0,1,0] op_sel_hi:[0,0,0] cbsz:4 blgp:2
	v_mfma_scale_f32_16x16x128_f8f6f4 v[46:49], v[218:221], v[178:183], v[46:49], v177, v244 op_sel:[0,1,0] op_sel_hi:[0,0,0] cbsz:4 blgp:2
	v_mfma_scale_f32_16x16x128_f8f6f4 v[30:33], v[222:225], v[178:183], v[30:33], v177, v244 op_sel:[0,1,0] op_sel_hi:[0,0,0] cbsz:4 blgp:2
	v_mfma_scale_f32_16x16x128_f8f6f4 v[18:21], v[226:229], v[178:183], v[238:241], v177, v244 op_sel:[0,1,0] op_sel_hi:[0,0,0] cbsz:4 blgp:2
	v_mfma_scale_f32_16x16x128_f8f6f4 v[10:13], v[230:233], v[178:183], v[14:17], v177, v244 op_sel:[0,1,0] op_sel_hi:[0,0,0] cbsz:4 blgp:2
	v_mfma_scale_f32_16x16x128_f8f6f4 v[90:93], v[202:205], v[184:189], v[90:93], v177, v245 op_sel:[0,1,0] op_sel_hi:[0,0,0] cbsz:4 blgp:2
	v_mfma_scale_f32_16x16x128_f8f6f4 v[74:77], v[206:209], v[184:189], v[74:77], v177, v245 op_sel:[0,1,0] op_sel_hi:[0,0,0] cbsz:4 blgp:2
	v_mfma_scale_f32_16x16x128_f8f6f4 v[58:61], v[210:213], v[184:189], v[58:61], v177, v245 op_sel:[0,1,0] op_sel_hi:[0,0,0] cbsz:4 blgp:2
	v_mfma_scale_f32_16x16x128_f8f6f4 v[42:45], v[214:217], v[184:189], v[42:45], v177, v245 op_sel:[0,1,0] op_sel_hi:[0,0,0] cbsz:4 blgp:2
	v_mfma_scale_f32_16x16x128_f8f6f4 v[26:29], v[218:221], v[184:189], v[26:29], v177, v245 op_sel:[0,1,0] op_sel_hi:[0,0,0] cbsz:4 blgp:2
	v_mfma_scale_f32_16x16x128_f8f6f4 v[14:17], v[222:225], v[184:189], v[190:193], v177, v245 op_sel:[0,1,0] op_sel_hi:[0,0,0] cbsz:4 blgp:2
	v_mfma_scale_f32_16x16x128_f8f6f4 v[6:9], v[226:229], v[184:189], v[198:201], v177, v245 op_sel:[0,1,0] op_sel_hi:[0,0,0] cbsz:4 blgp:2
	v_mfma_scale_f32_16x16x128_f8f6f4 v[2:5], v[230:233], v[184:189], v[194:197], v177, v245 op_sel:[0,1,0] op_sel_hi:[0,0,0] cbsz:4 blgp:2
	s_barrier
	s_add_i32 s59, s59, 2
	s_addk_i32 s60, 0x1000
	s_add_u32 s72, s72, 0x8000
	s_addc_u32 s73, s73, 0
	s_add_u32 s74, s74, 0x8000
	s_addc_u32 s75, s75, 0
	s_add_u32 s76, s76, 0x18000
	s_addc_u32 s77, s77, 0
	s_add_u32 s78, s78, 0x18000
	s_addc_u32 s79, s79, 0
	s_add_u32 s80, s80, 0x1000
	s_addc_u32 s81, s81, 0
	s_cmp_lt_u32 s59, 28
	s_cbranch_scc1 .LBB3_3
	ds_read_b128 v[154:157], v175
	ds_read_b128 v[186:189], v175 offset:256
	ds_read_b128 v[190:193], v175 offset:512
	ds_read_b128 v[194:197], v175 offset:768
	ds_read_b128 v[198:201], v175 offset:1024
	ds_read_b128 v[202:205], v175 offset:1280
	ds_read_b128 v[206:209], v175 offset:1536
	ds_read_b128 v[210:213], v175 offset:1792
	ds_read_b64 v[142:143], v171
	ds_read_b64 v[144:145], v171 offset:8
	ds_read_b64 v[146:147], v171 offset:16
	ds_read_b64 v[148:149], v174
	ds_read_b64 v[150:151], v174 offset:8
	ds_read_b64 v[152:153], v174 offset:16
	ds_read_b64 v[174:175], v173
	ds_read_b64 v[176:177], v173 offset:8
	ds_read_b64 v[178:179], v173 offset:16
	ds_read_b64 v[180:181], v172
	ds_read_b64 v[182:183], v172 offset:8
	ds_read_b64 v[184:185], v172 offset:16
	v_add_u32_e32 v171, 0x21000, v248
	v_add_u32_e32 v172, 0x21020, v248
	v_add_u32_e32 v173, 0x21040, v248
	v_add_u32_e32 v214, 0x21060, v248
	s_mov_b64 s[0:1], 0x7c000
	s_mov_b32 m0, s61
	ds_read_u16 v171, v171
	ds_read_u16 v215, v172
	ds_read_u16 v216, v173
	ds_read_u16 v214, v214
	v_lshl_add_u64 v[172:173], v[138:139], 0, s[0:1]
	s_mov_b64 s[0:1], 0x7e000
	v_lshl_add_u64 v[138:139], v[138:139], 0, s[0:1]
	s_mov_b32 m0, s58
	s_mov_b64 s[0:1], 0x174000
	v_lshl_add_u64 v[138:139], v[140:141], 0, s[0:1]
	v_lshl_add_u64 v[140:141], v[138:139], 0, s[16:17]
	s_mov_b32 m0, s57
	v_lshl_add_u64 v[130:131], s[14:15], 0, v[130:131]
	global_load_lds_dwordx4 v[140:141], off
	v_lshl_add_u64 v[140:141], v[138:139], 0, s[18:19]
	s_mov_b32 m0, s56
	v_lshl_add_u64 v[138:139], v[138:139], 0, s[20:21]
	global_load_lds_dwordx4 v[140:141], off
	s_mov_b32 m0, s55
	s_mov_b64 s[0:1], 0xf800
	global_load_lds_dwordx4 v[138:139], off
	v_lshl_add_u64 v[130:131], v[130:131], 0, s[0:1]
	s_add_i32 m0, s9, 0x21800
	s_waitcnt lgkmcnt(0)
	v_mov_b32_e32 v172, v216
	global_load_lds_dword v[130:131], off
	s_waitcnt vmcnt(6)
	s_waitcnt lgkmcnt(0)
	v_mov_b32_e32 v130, v171
	v_mov_b32_e32 v131, v215
	v_mov_b32_e32 v217, v214
	s_barrier
	v_mov_b32_e32 v161, 0x7f7f7f7f
	s_nop 1
	v_mfma_scale_f32_16x16x128_f8f6f4 v[126:129], v[154:157], v[142:147], v[126:129], v161, v130 op_sel_hi:[0,0,0] cbsz:4 blgp:2
	v_mfma_scale_f32_16x16x128_f8f6f4 v[122:125], v[186:189], v[142:147], v[122:125], v161, v130 op_sel_hi:[0,0,0] cbsz:4 blgp:2
	v_mfma_scale_f32_16x16x128_f8f6f4 v[114:117], v[190:193], v[142:147], v[114:117], v161, v130 op_sel_hi:[0,0,0] cbsz:4 blgp:2
	v_mfma_scale_f32_16x16x128_f8f6f4 v[102:105], v[194:197], v[142:147], v[102:105], v161, v130 op_sel_hi:[0,0,0] cbsz:4 blgp:2
	v_mfma_scale_f32_16x16x128_f8f6f4 v[86:89], v[198:201], v[142:147], v[86:89], v161, v130 op_sel_hi:[0,0,0] cbsz:4 blgp:2
	v_mfma_scale_f32_16x16x128_f8f6f4 v[70:73], v[202:205], v[142:147], v[70:73], v161, v130 op_sel_hi:[0,0,0] cbsz:4 blgp:2
	v_mfma_scale_f32_16x16x128_f8f6f4 v[54:57], v[206:209], v[142:147], v[54:57], v161, v130 op_sel_hi:[0,0,0] cbsz:4 blgp:2
	v_mfma_scale_f32_16x16x128_f8f6f4 v[38:41], v[210:213], v[142:147], v[38:41], v161, v130 op_sel_hi:[0,0,0] cbsz:4 blgp:2
	v_mfma_scale_f32_16x16x128_f8f6f4 v[118:121], v[154:157], v[148:153], v[118:121], v161, v131 op_sel_hi:[0,0,0] cbsz:4 blgp:2
	v_mfma_scale_f32_16x16x128_f8f6f4 v[110:113], v[186:189], v[148:153], v[110:113], v161, v131 op_sel_hi:[0,0,0] cbsz:4 blgp:2
	v_mfma_scale_f32_16x16x128_f8f6f4 v[98:101], v[190:193], v[148:153], v[98:101], v161, v131 op_sel_hi:[0,0,0] cbsz:4 blgp:2
	v_mfma_scale_f32_16x16x128_f8f6f4 v[82:85], v[194:197], v[148:153], v[82:85], v161, v131 op_sel_hi:[0,0,0] cbsz:4 blgp:2
	v_mfma_scale_f32_16x16x128_f8f6f4 v[66:69], v[198:201], v[148:153], v[66:69], v161, v131 op_sel_hi:[0,0,0] cbsz:4 blgp:2
	v_mfma_scale_f32_16x16x128_f8f6f4 v[50:53], v[202:205], v[148:153], v[50:53], v161, v131 op_sel_hi:[0,0,0] cbsz:4 blgp:2
	v_mfma_scale_f32_16x16x128_f8f6f4 v[34:37], v[206:209], v[148:153], v[34:37], v161, v131 op_sel_hi:[0,0,0] cbsz:4 blgp:2
	v_mfma_scale_f32_16x16x128_f8f6f4 v[138:141], v[210:213], v[148:153], v[22:25], v161, v131 op_sel_hi:[0,0,0] cbsz:4 blgp:2
	v_mfma_scale_f32_16x16x128_f8f6f4 v[106:109], v[154:157], v[174:179], v[106:109], v161, v172 op_sel_hi:[0,0,0] cbsz:4 blgp:2
	v_mfma_scale_f32_16x16x128_f8f6f4 v[94:97], v[186:189], v[174:179], v[94:97], v161, v172 op_sel_hi:[0,0,0] cbsz:4 blgp:2
	v_mfma_scale_f32_16x16x128_f8f6f4 v[78:81], v[190:193], v[174:179], v[78:81], v161, v172 op_sel_hi:[0,0,0] cbsz:4 blgp:2
	v_mfma_scale_f32_16x16x128_f8f6f4 v[62:65], v[194:197], v[174:179], v[62:65], v161, v172 op_sel_hi:[0,0,0] cbsz:4 blgp:2
	v_mfma_scale_f32_16x16x128_f8f6f4 v[46:49], v[198:201], v[174:179], v[46:49], v161, v172 op_sel_hi:[0,0,0] cbsz:4 blgp:2
	v_mfma_scale_f32_16x16x128_f8f6f4 v[142:145], v[206:209], v[174:179], v[18:21], v161, v172 op_sel_hi:[0,0,0] cbsz:4 blgp:2
	v_mfma_scale_f32_16x16x128_f8f6f4 v[146:149], v[210:213], v[174:179], v[10:13], v161, v172 op_sel_hi:[0,0,0] cbsz:4 blgp:2
	v_mfma_scale_f32_16x16x128_f8f6f4 v[90:93], v[154:157], v[180:185], v[90:93], v161, v217 op_sel_hi:[0,0,0] cbsz:4 blgp:2
	v_mfma_scale_f32_16x16x128_f8f6f4 v[74:77], v[186:189], v[180:185], v[74:77], v161, v217 op_sel_hi:[0,0,0] cbsz:4 blgp:2
	v_mfma_scale_f32_16x16x128_f8f6f4 v[58:61], v[190:193], v[180:185], v[58:61], v161, v217 op_sel_hi:[0,0,0] cbsz:4 blgp:2
	v_mfma_scale_f32_16x16x128_f8f6f4 v[150:153], v[202:205], v[180:185], v[14:17], v161, v217 op_sel_hi:[0,0,0] cbsz:4 blgp:2
	v_mfma_scale_f32_16x16x128_f8f6f4 v[30:33], v[202:205], v[174:179], v[30:33], v161, v172 op_sel_hi:[0,0,0] cbsz:4 blgp:2
	v_mfma_scale_f32_16x16x128_f8f6f4 v[42:45], v[194:197], v[180:185], v[42:45], v161, v217 op_sel_hi:[0,0,0] cbsz:4 blgp:2
	v_mfma_scale_f32_16x16x128_f8f6f4 v[26:29], v[198:201], v[180:185], v[26:29], v161, v217 op_sel_hi:[0,0,0] cbsz:4 blgp:2
	v_mfma_scale_f32_16x16x128_f8f6f4 v[172:175], v[206:209], v[180:185], v[6:9], v161, v217 op_sel_hi:[0,0,0] cbsz:4 blgp:2
	v_mfma_scale_f32_16x16x128_f8f6f4 v[176:179], v[210:213], v[180:185], v[2:5], v161, v217 op_sel_hi:[0,0,0] cbsz:4 blgp:2
	s_barrier
	ds_read_b64 v[2:3], v167
	ds_read_b64 v[4:5], v167 offset:8
	ds_read_b64 v[6:7], v167 offset:16
	ds_read_b64 v[8:9], v170
	ds_read_b64 v[10:11], v170 offset:8
	ds_read_b64 v[12:13], v170 offset:16
	ds_read_b64 v[14:15], v169
	ds_read_b64 v[16:17], v169 offset:8
	ds_read_b64 v[18:19], v169 offset:16
	s_mov_b64 s[0:1], 0x175800
	s_mov_b32 m0, s52
	ds_read_b64 v[20:21], v168
	ds_read_b64 v[22:23], v168 offset:8
	ds_read_b64 v[24:25], v168 offset:16
	v_lshl_add_u64 v[130:131], v[132:133], 0, s[0:1]
	global_load_lds_dwordx4 v[130:131], off
	v_lshl_add_u64 v[130:131], v[134:135], 0, s[0:1]
	s_mov_b32 m0, s50
	v_lshrrev_b32_e32 v167, 8, v216
	global_load_lds_dwordx4 v[130:131], off
	v_lshl_add_u64 v[130:131], v[136:137], 0, s[0:1]
	s_mov_b32 m0, s49
	v_lshrrev_b32_e32 v168, 8, v214
	global_load_lds_dwordx4 v[130:131], off
	s_waitcnt vmcnt(3)
	s_waitcnt lgkmcnt(0)
	v_lshrrev_b32_e32 v130, 8, v171
	v_lshrrev_b32_e32 v131, 8, v215
	s_barrier
	v_mfma_scale_f32_16x16x128_f8f6f4 v[126:129], v[154:157], v[2:7], v[126:129], v161, v130 op_sel_hi:[0,0,0] cbsz:4 blgp:2
	v_mfma_scale_f32_16x16x128_f8f6f4 v[122:125], v[186:189], v[2:7], v[122:125], v161, v130 op_sel_hi:[0,0,0] cbsz:4 blgp:2
	v_mfma_scale_f32_16x16x128_f8f6f4 v[114:117], v[190:193], v[2:7], v[114:117], v161, v130 op_sel_hi:[0,0,0] cbsz:4 blgp:2
	v_mfma_scale_f32_16x16x128_f8f6f4 v[102:105], v[194:197], v[2:7], v[102:105], v161, v130 op_sel_hi:[0,0,0] cbsz:4 blgp:2
	v_mfma_scale_f32_16x16x128_f8f6f4 v[86:89], v[198:201], v[2:7], v[86:89], v161, v130 op_sel_hi:[0,0,0] cbsz:4 blgp:2
	v_mfma_scale_f32_16x16x128_f8f6f4 v[70:73], v[202:205], v[2:7], v[70:73], v161, v130 op_sel_hi:[0,0,0] cbsz:4 blgp:2
	v_mfma_scale_f32_16x16x128_f8f6f4 v[54:57], v[206:209], v[2:7], v[54:57], v161, v130 op_sel_hi:[0,0,0] cbsz:4 blgp:2
	v_mfma_scale_f32_16x16x128_f8f6f4 v[38:41], v[210:213], v[2:7], v[38:41], v161, v130 op_sel_hi:[0,0,0] cbsz:4 blgp:2
	v_mfma_scale_f32_16x16x128_f8f6f4 v[118:121], v[154:157], v[8:13], v[118:121], v161, v131 op_sel_hi:[0,0,0] cbsz:4 blgp:2
	v_mfma_scale_f32_16x16x128_f8f6f4 v[110:113], v[186:189], v[8:13], v[110:113], v161, v131 op_sel_hi:[0,0,0] cbsz:4 blgp:2
	v_mfma_scale_f32_16x16x128_f8f6f4 v[98:101], v[190:193], v[8:13], v[98:101], v161, v131 op_sel_hi:[0,0,0] cbsz:4 blgp:2
	v_mfma_scale_f32_16x16x128_f8f6f4 v[82:85], v[194:197], v[8:13], v[82:85], v161, v131 op_sel_hi:[0,0,0] cbsz:4 blgp:2
	v_mfma_scale_f32_16x16x128_f8f6f4 v[66:69], v[198:201], v[8:13], v[66:69], v161, v131 op_sel_hi:[0,0,0] cbsz:4 blgp:2
	v_mfma_scale_f32_16x16x128_f8f6f4 v[50:53], v[202:205], v[8:13], v[50:53], v161, v131 op_sel_hi:[0,0,0] cbsz:4 blgp:2
	v_mfma_scale_f32_16x16x128_f8f6f4 v[34:37], v[206:209], v[8:13], v[34:37], v161, v131 op_sel_hi:[0,0,0] cbsz:4 blgp:2
	v_mfma_scale_f32_16x16x128_f8f6f4 v[130:133], v[210:213], v[8:13], v[138:141], v161, v131 op_sel_hi:[0,0,0] cbsz:4 blgp:2
	v_mfma_scale_f32_16x16x128_f8f6f4 v[106:109], v[154:157], v[14:19], v[106:109], v161, v167 op_sel_hi:[0,0,0] cbsz:4 blgp:2
	v_mfma_scale_f32_16x16x128_f8f6f4 v[94:97], v[186:189], v[14:19], v[94:97], v161, v167 op_sel_hi:[0,0,0] cbsz:4 blgp:2
	v_mfma_scale_f32_16x16x128_f8f6f4 v[78:81], v[190:193], v[14:19], v[78:81], v161, v167 op_sel_hi:[0,0,0] cbsz:4 blgp:2
	v_mfma_scale_f32_16x16x128_f8f6f4 v[62:65], v[194:197], v[14:19], v[62:65], v161, v167 op_sel_hi:[0,0,0] cbsz:4 blgp:2
	v_mfma_scale_f32_16x16x128_f8f6f4 v[46:49], v[198:201], v[14:19], v[46:49], v161, v167 op_sel_hi:[0,0,0] cbsz:4 blgp:2
	v_mfma_scale_f32_16x16x128_f8f6f4 v[134:137], v[206:209], v[14:19], v[142:145], v161, v167 op_sel_hi:[0,0,0] cbsz:4 blgp:2
	v_mfma_scale_f32_16x16x128_f8f6f4 v[138:141], v[210:213], v[14:19], v[146:149], v161, v167 op_sel_hi:[0,0,0] cbsz:4 blgp:2
	v_mfma_scale_f32_16x16x128_f8f6f4 v[90:93], v[154:157], v[20:25], v[90:93], v161, v168 op_sel_hi:[0,0,0] cbsz:4 blgp:2
	v_mfma_scale_f32_16x16x128_f8f6f4 v[58:61], v[190:193], v[20:25], v[58:61], v161, v168 op_sel_hi:[0,0,0] cbsz:4 blgp:2
	v_mfma_scale_f32_16x16x128_f8f6f4 v[142:145], v[202:205], v[20:25], v[150:153], v161, v168 op_sel_hi:[0,0,0] cbsz:4 blgp:2
	v_mfma_scale_f32_16x16x128_f8f6f4 v[146:149], v[206:209], v[20:25], v[172:175], v161, v168 op_sel_hi:[0,0,0] cbsz:4 blgp:2
	v_mfma_scale_f32_16x16x128_f8f6f4 v[150:153], v[210:213], v[20:25], v[176:179], v161, v168 op_sel_hi:[0,0,0] cbsz:4 blgp:2
	v_mfma_scale_f32_16x16x128_f8f6f4 v[30:33], v[202:205], v[14:19], v[30:33], v161, v167 op_sel_hi:[0,0,0] cbsz:4 blgp:2
	v_mfma_scale_f32_16x16x128_f8f6f4 v[236:239], v[186:189], v[20:25], v[74:77], v161, v168 op_sel_hi:[0,0,0] cbsz:4 blgp:2
	v_mfma_scale_f32_16x16x128_f8f6f4 v[42:45], v[194:197], v[20:25], v[42:45], v161, v168 op_sel_hi:[0,0,0] cbsz:4 blgp:2
	v_mfma_scale_f32_16x16x128_f8f6f4 v[26:29], v[198:201], v[20:25], v[26:29], v161, v168 op_sel_hi:[0,0,0] cbsz:4 blgp:2
	s_barrier
	ds_read_b128 v[168:171], v166
	ds_read_b128 v[172:175], v166 offset:256
	ds_read_b128 v[176:179], v166 offset:512
	ds_read_b128 v[180:183], v166 offset:768
	ds_read_b128 v[184:187], v166 offset:1024
	ds_read_b128 v[188:191], v166 offset:1280
	ds_read_b128 v[192:195], v166 offset:1536
	ds_read_b128 v[196:199], v166 offset:1792
	ds_read_b64 v[2:3], v162
	ds_read_b64 v[4:5], v162 offset:8
	ds_read_b64 v[6:7], v162 offset:16
	ds_read_b64 v[8:9], v165
	ds_read_b64 v[10:11], v165 offset:8
	ds_read_b64 v[12:13], v165 offset:16
	ds_read_b64 v[14:15], v164
	ds_read_b64 v[16:17], v164 offset:8
	ds_read_b64 v[18:19], v164 offset:16
	ds_read_b64 v[20:21], v163
	ds_read_b64 v[22:23], v163 offset:8
	ds_read_b64 v[24:25], v163 offset:16
	v_add_u32_e32 v154, 0x21800, v248
	v_add_u32_e32 v155, 0x21820, v248
	v_add_u32_e32 v156, 0x21840, v248
	v_add_u32_e32 v157, 0x21860, v248
	ds_read_u16 v166, v154
	ds_read_u16 v167, v155
	ds_read_u16 v74, v156
	ds_read_u16 v75, v157
	s_waitcnt vmcnt(0)
	s_waitcnt lgkmcnt(0)
	s_waitcnt lgkmcnt(0)
	v_mov_b32_e32 v76, v166
	v_mov_b32_e32 v77, v167
	v_mov_b32_e32 v228, v74
	v_mov_b32_e32 v252, v75
	s_barrier
	v_mfma_scale_f32_16x16x128_f8f6f4 v[126:129], v[168:171], v[2:7], v[126:129], v161, v76 op_sel_hi:[0,0,0] cbsz:4 blgp:2
	v_mfma_scale_f32_16x16x128_f8f6f4 v[122:125], v[172:175], v[2:7], v[122:125], v161, v76 op_sel_hi:[0,0,0] cbsz:4 blgp:2
	v_mfma_scale_f32_16x16x128_f8f6f4 v[114:117], v[176:179], v[2:7], v[114:117], v161, v76 op_sel_hi:[0,0,0] cbsz:4 blgp:2
	v_mfma_scale_f32_16x16x128_f8f6f4 v[102:105], v[180:183], v[2:7], v[102:105], v161, v76 op_sel_hi:[0,0,0] cbsz:4 blgp:2
	v_mfma_scale_f32_16x16x128_f8f6f4 v[86:89], v[184:187], v[2:7], v[86:89], v161, v76 op_sel_hi:[0,0,0] cbsz:4 blgp:2
	v_mfma_scale_f32_16x16x128_f8f6f4 v[70:73], v[188:191], v[2:7], v[70:73], v161, v76 op_sel_hi:[0,0,0] cbsz:4 blgp:2
	v_mfma_scale_f32_16x16x128_f8f6f4 v[54:57], v[192:195], v[2:7], v[54:57], v161, v76 op_sel_hi:[0,0,0] cbsz:4 blgp:2
	v_mfma_scale_f32_16x16x128_f8f6f4 v[154:157], v[196:199], v[2:7], v[38:41], v161, v76 op_sel_hi:[0,0,0] cbsz:4 blgp:2
	v_mfma_scale_f32_16x16x128_f8f6f4 v[118:121], v[168:171], v[8:13], v[118:121], v161, v77 op_sel_hi:[0,0,0] cbsz:4 blgp:2
	v_mfma_scale_f32_16x16x128_f8f6f4 v[82:85], v[180:183], v[8:13], v[82:85], v161, v77 op_sel_hi:[0,0,0] cbsz:4 blgp:2
	v_mfma_scale_f32_16x16x128_f8f6f4 v[66:69], v[184:187], v[8:13], v[66:69], v161, v77 op_sel_hi:[0,0,0] cbsz:4 blgp:2
	v_mfma_scale_f32_16x16x128_f8f6f4 v[50:53], v[188:191], v[8:13], v[50:53], v161, v77 op_sel_hi:[0,0,0] cbsz:4 blgp:2
	v_mfma_scale_f32_16x16x128_f8f6f4 v[130:133], v[196:199], v[8:13], v[130:133], v161, v77 op_sel_hi:[0,0,0] cbsz:4 blgp:2
	v_mfma_scale_f32_16x16x128_f8f6f4 v[62:65], v[180:183], v[14:19], v[62:65], v161, v228 op_sel_hi:[0,0,0] cbsz:4 blgp:2
	v_mfma_scale_f32_16x16x128_f8f6f4 v[46:49], v[184:187], v[14:19], v[46:49], v161, v228 op_sel_hi:[0,0,0] cbsz:4 blgp:2
	v_mfma_scale_f32_16x16x128_f8f6f4 v[58:61], v[176:179], v[20:25], v[58:61], v161, v252 op_sel_hi:[0,0,0] cbsz:4 blgp:2
	v_mfma_scale_f32_16x16x128_f8f6f4 v[162:165], v[172:175], v[8:13], v[110:113], v161, v77 op_sel_hi:[0,0,0] cbsz:4 blgp:2
	v_mfma_scale_f32_16x16x128_f8f6f4 v[200:203], v[176:179], v[8:13], v[98:101], v161, v77 op_sel_hi:[0,0,0] cbsz:4 blgp:2
	v_mfma_scale_f32_16x16x128_f8f6f4 v[204:207], v[192:195], v[8:13], v[34:37], v161, v77 op_sel_hi:[0,0,0] cbsz:4 blgp:2
	v_mfma_scale_f32_16x16x128_f8f6f4 v[208:211], v[168:171], v[14:19], v[106:109], v161, v228 op_sel_hi:[0,0,0] cbsz:4 blgp:2
	v_mfma_scale_f32_16x16x128_f8f6f4 v[212:215], v[172:175], v[14:19], v[94:97], v161, v228 op_sel_hi:[0,0,0] cbsz:4 blgp:2
	v_mfma_scale_f32_16x16x128_f8f6f4 v[216:219], v[176:179], v[14:19], v[78:81], v161, v228 op_sel_hi:[0,0,0] cbsz:4 blgp:2
	v_mfma_scale_f32_16x16x128_f8f6f4 v[220:223], v[188:191], v[14:19], v[30:33], v161, v228 op_sel_hi:[0,0,0] cbsz:4 blgp:2
	v_mfma_scale_f32_16x16x128_f8f6f4 v[224:227], v[192:195], v[14:19], v[134:137], v161, v228 op_sel_hi:[0,0,0] cbsz:4 blgp:2
	v_mfma_scale_f32_16x16x128_f8f6f4 v[228:231], v[196:199], v[14:19], v[138:141], v161, v228 op_sel_hi:[0,0,0] cbsz:4 blgp:2
	v_mfma_scale_f32_16x16x128_f8f6f4 v[232:235], v[168:171], v[20:25], v[90:93], v161, v252 op_sel_hi:[0,0,0] cbsz:4 blgp:2
	v_mfma_scale_f32_16x16x128_f8f6f4 v[236:239], v[172:175], v[20:25], v[236:239], v161, v252 op_sel_hi:[0,0,0] cbsz:4 blgp:2
	v_mfma_scale_f32_16x16x128_f8f6f4 v[42:45], v[180:183], v[20:25], v[42:45], v161, v252 op_sel_hi:[0,0,0] cbsz:4 blgp:2
	v_mfma_scale_f32_16x16x128_f8f6f4 v[240:243], v[184:187], v[20:25], v[26:29], v161, v252 op_sel_hi:[0,0,0] cbsz:4 blgp:2
	v_mfma_scale_f32_16x16x128_f8f6f4 v[244:247], v[188:191], v[20:25], v[142:145], v161, v252 op_sel_hi:[0,0,0] cbsz:4 blgp:2
	v_mfma_scale_f32_16x16x128_f8f6f4 v[248:251], v[192:195], v[20:25], v[146:149], v161, v252 op_sel_hi:[0,0,0] cbsz:4 blgp:2
	v_mfma_scale_f32_16x16x128_f8f6f4 v[252:255], v[196:199], v[20:25], v[150:153], v161, v252 op_sel_hi:[0,0,0] cbsz:4 blgp:2
	s_barrier
	ds_read_b64 v[18:19], v1
	ds_read_b64 v[20:21], v1 offset:8
	ds_read_b64 v[22:23], v1 offset:16
	ds_read_b64 v[24:25], v160
	ds_read_b64 v[26:27], v160 offset:8
	ds_read_b64 v[28:29], v160 offset:16
	ds_read_b64 v[30:31], v159
	ds_read_b64 v[32:33], v159 offset:8
	ds_read_b64 v[34:35], v159 offset:16
	ds_read_b64 v[36:37], v158
	ds_read_b64 v[38:39], v158 offset:8
	ds_read_b64 v[40:41], v158 offset:16
	s_waitcnt lgkmcnt(0)
	v_lshrrev_b32_e32 v1, 8, v166
	v_lshrrev_b32_e32 v76, 8, v167
	v_lshrrev_b32_e32 v112, 8, v74
	v_lshrrev_b32_e32 v160, 8, v75
	s_barrier
	v_mfma_scale_f32_16x16x128_f8f6f4 v[14:17], v[168:171], v[18:23], v[126:129], v161, v1 op_sel_hi:[0,0,0] cbsz:4 blgp:2
	v_mfma_scale_f32_16x16x128_f8f6f4 v[10:13], v[172:175], v[18:23], v[122:125], v161, v1 op_sel_hi:[0,0,0] cbsz:4 blgp:2
	v_mfma_scale_f32_16x16x128_f8f6f4 v[6:9], v[176:179], v[18:23], v[114:117], v161, v1 op_sel_hi:[0,0,0] cbsz:4 blgp:2
	v_mfma_scale_f32_16x16x128_f8f6f4 v[2:5], v[180:183], v[18:23], v[102:105], v161, v1 op_sel_hi:[0,0,0] cbsz:4 blgp:2
	v_mfma_scale_f32_16x16x128_f8f6f4 v[108:111], v[184:187], v[18:23], v[86:89], v161, v1 op_sel_hi:[0,0,0] cbsz:4 blgp:2
	v_mfma_scale_f32_16x16x128_f8f6f4 v[104:107], v[188:191], v[18:23], v[70:73], v161, v1 op_sel_hi:[0,0,0] cbsz:4 blgp:2
	v_mfma_scale_f32_16x16x128_f8f6f4 v[100:103], v[192:195], v[18:23], v[54:57], v161, v1 op_sel_hi:[0,0,0] cbsz:4 blgp:2
	v_mfma_scale_f32_16x16x128_f8f6f4 v[96:99], v[196:199], v[18:23], v[154:157], v161, v1 op_sel_hi:[0,0,0] cbsz:4 blgp:2
	v_mfma_scale_f32_16x16x128_f8f6f4 v[156:159], v[168:171], v[24:29], v[118:121], v161, v76 op_sel_hi:[0,0,0] cbsz:4 blgp:2
	v_mfma_scale_f32_16x16x128_f8f6f4 v[152:155], v[172:175], v[24:29], v[162:165], v161, v76 op_sel_hi:[0,0,0] cbsz:4 blgp:2
	v_mfma_scale_f32_16x16x128_f8f6f4 v[148:151], v[176:179], v[24:29], v[200:203], v161, v76 op_sel_hi:[0,0,0] cbsz:4 blgp:2
	v_mfma_scale_f32_16x16x128_f8f6f4 v[144:147], v[180:183], v[24:29], v[82:85], v161, v76 op_sel_hi:[0,0,0] cbsz:4 blgp:2
	v_mfma_scale_f32_16x16x128_f8f6f4 v[92:95], v[184:187], v[24:29], v[66:69], v161, v76 op_sel_hi:[0,0,0] cbsz:4 blgp:2
	v_mfma_scale_f32_16x16x128_f8f6f4 v[88:91], v[188:191], v[24:29], v[50:53], v161, v76 op_sel_hi:[0,0,0] cbsz:4 blgp:2
	v_mfma_scale_f32_16x16x128_f8f6f4 v[84:87], v[192:195], v[24:29], v[204:207], v161, v76 op_sel_hi:[0,0,0] cbsz:4 blgp:2
	v_mfma_scale_f32_16x16x128_f8f6f4 v[80:83], v[196:199], v[24:29], v[130:133], v161, v76 op_sel_hi:[0,0,0] cbsz:4 blgp:2
	v_mfma_scale_f32_16x16x128_f8f6f4 v[140:143], v[168:171], v[30:35], v[208:211], v161, v112 op_sel_hi:[0,0,0] cbsz:4 blgp:2
	v_mfma_scale_f32_16x16x128_f8f6f4 v[136:139], v[172:175], v[30:35], v[212:215], v161, v112 op_sel_hi:[0,0,0] cbsz:4 blgp:2
	v_mfma_scale_f32_16x16x128_f8f6f4 v[132:135], v[176:179], v[30:35], v[216:219], v161, v112 op_sel_hi:[0,0,0] cbsz:4 blgp:2
	v_mfma_scale_f32_16x16x128_f8f6f4 v[128:131], v[180:183], v[30:35], v[62:65], v161, v112 op_sel_hi:[0,0,0] cbsz:4 blgp:2
	v_mfma_scale_f32_16x16x128_f8f6f4 v[76:79], v[184:187], v[30:35], v[46:49], v161, v112 op_sel_hi:[0,0,0] cbsz:4 blgp:2
	v_mfma_scale_f32_16x16x128_f8f6f4 v[72:75], v[188:191], v[30:35], v[220:223], v161, v112 op_sel_hi:[0,0,0] cbsz:4 blgp:2
	v_mfma_scale_f32_16x16x128_f8f6f4 v[68:71], v[192:195], v[30:35], v[224:227], v161, v112 op_sel_hi:[0,0,0] cbsz:4 blgp:2
	v_mfma_scale_f32_16x16x128_f8f6f4 v[64:67], v[196:199], v[30:35], v[228:231], v161, v112 op_sel_hi:[0,0,0] cbsz:4 blgp:2
	v_mfma_scale_f32_16x16x128_f8f6f4 v[124:127], v[168:171], v[36:41], v[232:235], v161, v160 op_sel_hi:[0,0,0] cbsz:4 blgp:2
	v_mfma_scale_f32_16x16x128_f8f6f4 v[120:123], v[172:175], v[36:41], v[236:239], v161, v160 op_sel_hi:[0,0,0] cbsz:4 blgp:2
	v_mfma_scale_f32_16x16x128_f8f6f4 v[116:119], v[176:179], v[36:41], v[58:61], v161, v160 op_sel_hi:[0,0,0] cbsz:4 blgp:2
	v_mfma_scale_f32_16x16x128_f8f6f4 v[112:115], v[180:183], v[36:41], v[42:45], v161, v160 op_sel_hi:[0,0,0] cbsz:4 blgp:2
	v_mfma_scale_f32_16x16x128_f8f6f4 v[60:63], v[184:187], v[36:41], v[240:243], v161, v160 op_sel_hi:[0,0,0] cbsz:4 blgp:2
	v_mfma_scale_f32_16x16x128_f8f6f4 v[56:59], v[188:191], v[36:41], v[244:247], v161, v160 op_sel_hi:[0,0,0] cbsz:4 blgp:2
	v_mfma_scale_f32_16x16x128_f8f6f4 v[52:55], v[192:195], v[36:41], v[248:251], v161, v160 op_sel_hi:[0,0,0] cbsz:4 blgp:2
	v_mfma_scale_f32_16x16x128_f8f6f4 v[48:51], v[196:199], v[36:41], v[252:255], v161, v160 op_sel_hi:[0,0,0] cbsz:4 blgp:2
	s_barrier
	s_cmpk_gt_u32 s33, 0xff
	s_cbranch_scc1 .LBB3_6
	s_barrier

	.amdhsa_kernel _Z6mxgemmILi1ELi4096ELi4EEvPKcS1_PKfS3_Pvi
		.amdhsa_group_segment_fixed_size 0
		.amdhsa_private_segment_fixed_size 0
		.amdhsa_kernarg_size 44
		.amdhsa_user_sgpr_count 2
		.amdhsa_user_sgpr_dispatch_ptr 0
		.amdhsa_user_sgpr_queue_ptr 0
		.amdhsa_user_sgpr_kernarg_segment_ptr 1
		.amdhsa_user_sgpr_dispatch_id 0
		.amdhsa_user_sgpr_kernarg_preload_length 0
		.amdhsa_user_sgpr_kernarg_preload_offset 0
		.amdhsa_user_sgpr_private_segment_size 0
		.amdhsa_uses_dynamic_stack 0
		.amdhsa_enable_private_segment 0
		.amdhsa_system_sgpr_workgroup_id_x 1
		.amdhsa_system_sgpr_workgroup_id_y 0
		.amdhsa_system_sgpr_workgroup_id_z 0
		.amdhsa_system_sgpr_workgroup_info 0
		.amdhsa_system_vgpr_workitem_id 0
		.amdhsa_next_free_vgpr 256
		.amdhsa_next_free_sgpr 84
		.amdhsa_accum_offset 256
		.amdhsa_reserve_vcc 1
		.amdhsa_float_round_mode_32 0
		.amdhsa_float_round_mode_16_64 0
		.amdhsa_float_denorm_mode_32 3
		.amdhsa_float_denorm_mode_16_64 3
		.amdhsa_dx10_clamp 1
		.amdhsa_ieee_mode 1
		.amdhsa_fp16_overflow 0
		.amdhsa_tg_split 0
		.amdhsa_exception_fp_ieee_invalid_op 0
		.amdhsa_exception_fp_denorm_src 0
		.amdhsa_exception_fp_ieee_div_zero 0
		.amdhsa_exception_fp_ieee_overflow 0
		.amdhsa_exception_fp_ieee_underflow 0
		.amdhsa_exception_fp_ieee_inexact 0
		.amdhsa_exception_int_div_zero 0
	.end_amdhsa_kernel
